# baseline (speedup 1.0000x reference)
.Lmy_rx:
	v_and_b32_e32 v212, 3, v177
	v_mad_u32_u24 v213, v212, v209, v208
	v_mad_u32_u24 v214, v212, v211, v210
	global_load_dword v64, v213, s[66:67] sc1
	global_load_dword v183, v214, s[66:67] sc1
	v_cmp_eq_u32_e64 s[10:11], 0, v177
	v_cmp_ne_u32_e32 vcc, 0, v177
	s_and_saveexec_b64 s[12:13], vcc
	s_cbranch_execz .Lk_291
	v_mul_f32_e32 v60, v161, v59
	v_fma_f32 v46, v167, v52, 1.0
	v_mov_b32_e32 v61, v53
	v_pk_mul_f32 v[52:53], v[60:61], v[46:47]
	v_add_u32_e32 v12, -1, v177
	v_pk_fma_f32 v[52:53], v[58:59], s[26:27], v[52:53]
	v_cvt_f64_f32_e32 v[58:59], v59
	v_fmac_f64_e32 v[58:59], s[28:29], v[44:45]
	v_cvt_f64_f32_e32 v[44:45], v57
	v_mul_f32_e32 v62, v162, v57
	v_fma_f32 v50, v168, v50, 1.0
	v_mov_b32_e32 v63, v51
	v_mov_b32_e32 v51, v47
	v_fmac_f64_e32 v[44:45], s[28:29], v[48:49]
	v_cmp_eq_u32_e32 vcc, s33, v12
	v_pk_mul_f32 v[50:51], v[62:63], v[50:51]
	v_mov_b64_e32 v[48:49], v[44:45]
	v_cndmask_b32_e32 v39, v39, v45, vcc
	v_cndmask_b32_e32 v38, v38, v44, vcc
	v_cndmask_b32_e32 v37, v37, v59, vcc
	v_cndmask_b32_e32 v36, v36, v58, vcc
	v_cmp_eq_u32_e32 vcc, s69, v177
	v_pk_fma_f32 v[50:51], v[56:57], s[26:27], v[50:51]
	s_nop 0
	v_cndmask_b32_e32 v5, v5, v45, vcc
	v_cndmask_b32_e32 v4, v4, v44, vcc
	v_cndmask_b32_e32 v7, v7, v59, vcc
	v_cndmask_b32_e32 v6, v6, v58, vcc
	v_mov_b64_e32 v[44:45], v[58:59]
.Lk_291:
	s_or_b64 exec, exec, s[12:13]
	v_add_f32_e32 v216, 1.0, v52
	v_add_f32_e32 v217, 1.0, v50
	v_lshlrev_b32_e32 v215, 9, v177
	v_cmp_neq_f32_e32 vcc, 0, v216
	v_and_b32_e32 v215, 0x1e00, v215
	v_or_b32_e32 v250, v215, v160
	v_cndmask_b32_e32 v216, v173, v216, vcc
	v_cmp_neq_f32_e32 vcc, 0, v217
	v_or_b32_e32 v251, v215, v164
	v_lshlrev_b32_e32 v250, 3, v250
	v_cndmask_b32_e32 v217, v173, v217, vcc
	v_lshlrev_b32_e32 v251, 3, v251
	s_mov_b32 s90, 0
	s_xor_b64 s[50:51], s[44:45], -1
	v_add_u32_e32 v12, 1, v177
	s_mov_b64 s[12:13], -1
	s_waitcnt vmcnt(0)
	v_mov_b32_e32 v46, v183
	s_and_saveexec_b64 s[48:49], s[50:51]
	s_cbranch_execz .Lk_303
